# gemm role: W weight image staged with direct global->LDS loads (global_load_lds_dwordx4) instead of VGPR staging + ds_write
# speedup vs baseline: 1.0075x; 1.0075x over previous
.LBB1_69:
	s_and_b64 vcc, exec, s[4:5]
	s_cbranch_vccz .LBB1_79
	v_lshrrev_b32_e32 v2, 2, v0
	s_load_dwordx4 s[4:7], s[0:1], 0x0
	v_and_b32_e32 v2, 0x70, v2
	v_and_b32_e32 v1, 15, v0
	v_lshl_or_b32 v35, s2, 7, v2
	v_or_b32_e32 v34, v35, v1
	v_min_u32_e32 v2, 0xc34f, v34
	v_bfe_u32 v40, v0, 4, 2
	v_lshlrev_b32_e32 v36, 9, v2
	v_mov_b32_e32 v37, 0
	s_waitcnt vmcnt(0) lgkmcnt(0)
	v_lshl_add_u64 v[2:3], s[4:5], 0, v[36:37]
	v_lshlrev_b32_e32 v36, 5, v40
	v_lshl_add_u64 v[54:55], v[2:3], 0, v[36:37]
	global_load_dwordx4 v[30:33], v[54:55], off offset:16 nt
	global_load_dwordx4 v[18:21], v[54:55], off nt
	global_load_dwordx4 v[14:17], v[54:55], off offset:144 nt
	global_load_dwordx4 v[10:13], v[54:55], off offset:128 nt
	global_load_dwordx4 v[6:9], v[54:55], off offset:272 nt
	global_load_dwordx4 v[2:5], v[54:55], off offset:256 nt
	v_readfirstlane_b32 s20, v0
	v_lshlrev_b32_e32 v36, 4, v0
	s_lshr_b32 s20, s20, 6
	s_lshl_b32 s20, s20, 10
	s_mov_b32 m0, s20
	v_add_u32_e32 v42, 0x2000, v36
	global_load_lds_dwordx4 v36, s[6:7]
	s_add_i32 s21, s20, 0x2000
	s_mov_b32 m0, s21
	v_add_u32_e32 v43, 0x4000, v36
	global_load_lds_dwordx4 v42, s[6:7]
	s_add_i32 s21, s20, 0x4000
	s_mov_b32 m0, s21
	v_add_u32_e32 v44, 0x6000, v36
	global_load_lds_dwordx4 v43, s[6:7]
	s_add_i32 s21, s20, 0x6000
	s_mov_b32 m0, s21
	v_add_u32_e32 v45, 0x8000, v36
	global_load_lds_dwordx4 v44, s[6:7]
	s_movk_i32 s2, 0x190
	v_cmp_gt_u32_e32 vcc, s2, v0
	s_add_i32 s21, s20, 0x8000
	s_mov_b32 m0, s21
	s_and_saveexec_b64 s[2:3], vcc
	global_load_lds_dwordx4 v45, s[6:7]
	s_or_b64 exec, exec, s[2:3]
	global_load_dwordx4 v[26:29], v[54:55], off offset:400 nt
	global_load_dwordx4 v[22:25], v[54:55], off offset:384 nt
	s_waitcnt vmcnt(2)
	s_mov_b32 s2, 0xc350
	v_cmp_gt_u32_e32 vcc, s2, v35
	s_waitcnt lgkmcnt(0)
	s_barrier
	s_and_saveexec_b64 s[2:3], vcc
	s_cbranch_execz .LBB1_79
	v_lshlrev_b32_e32 v36, 3, v40
	v_mul_u32_u24_e32 v1, 0x110, v1
	v_lshl_add_u32 v37, v36, 1, v1
	ds_read_b128 v[42:45], v37
	v_cvt_pk_f16_f32 v33, v32, v33
	v_cvt_pk_f16_f32 v32, v30, v31
	v_cvt_pk_f16_f32 v31, v20, v21
	v_cvt_pk_f16_f32 v30, v18, v19
	ds_read_b128 v[18:21], v37 offset:64
	v_cvt_pk_f16_f32 v17, v16, v17
	v_cvt_pk_f16_f32 v16, v14, v15
	v_cvt_pk_f16_f32 v15, v12, v13
	v_cvt_pk_f16_f32 v14, v10, v11
	ds_read_b128 v[10:13], v37 offset:128
	ds_read_b128 v[46:49], v37 offset:192
	s_waitcnt lgkmcnt(3)
	v_mfma_f32_16x16x32_f16 v[42:45], v[42:45], v[30:33], 0
	v_cvt_pk_f16_f32 v9, v8, v9
	v_cvt_pk_f16_f32 v8, v6, v7
	v_cvt_pk_f16_f32 v7, v4, v5
	s_waitcnt lgkmcnt(2)
	v_mfma_f32_16x16x32_f16 v[18:21], v[18:21], v[14:17], v[42:45]
	v_cvt_pk_f16_f32 v6, v2, v3
	s_waitcnt vmcnt(0)
	v_cvt_pk_f16_f32 v3, v24, v25
	v_cvt_pk_f16_f32 v2, v22, v23
	s_waitcnt lgkmcnt(1)
	v_mfma_f32_16x16x32_f16 v[10:13], v[10:13], v[6:9], v[18:21]
	ds_read_b128 v[22:25], v37 offset:4416
	v_cvt_pk_f16_f32 v5, v28, v29
	v_cvt_pk_f16_f32 v4, v26, v27
	ds_read_b128 v[18:21], v37 offset:4352
	s_waitcnt lgkmcnt(0)
	v_mfma_f32_16x16x32_f16 v[18:21], v[18:21], v[30:33], 0
	ds_read_b128 v[26:29], v37 offset:4480
	ds_read_b128 v[42:45], v37 offset:8832
	ds_read_b128 v[50:53], v37 offset:17536
	v_mfma_f32_16x16x32_f16 v[18:21], v[22:25], v[14:17], v[18:21]
	ds_read_b128 v[22:25], v37 offset:4544
	ds_read_b128 v[54:57], v37 offset:21888
	v_mov_b32_e32 v35, 0
	s_waitcnt lgkmcnt(4)
	v_mfma_f32_16x16x32_f16 v[18:21], v[26:29], v[6:9], v[18:21]
	ds_read_b128 v[26:29], v37 offset:8704
	v_mov_b32_e32 v62, v35
	v_mov_b32_e32 v63, v35
	s_waitcnt lgkmcnt(2)
	v_mfma_f32_16x16x32_f16 v[18:21], v[22:25], v[2:5], v[18:21]
	ds_read_b128 v[22:25], v37 offset:8768
	s_load_dwordx2 s[2:3], s[0:1], 0x10
	v_lshrrev_b32_e32 v1, 4, v0
	s_waitcnt lgkmcnt(0)
	v_mfma_f32_16x16x32_f16 v[26:29], v[26:29], v[30:33], 0
	v_lshlrev_b64 v[38:39], 7, v[34:35]
	s_nop 1
	v_cvt_pk_fp8_f32 v63, v18, v19
	v_lshlrev_b32_e32 v1, 2, v1
	v_mfma_f32_16x16x32_f16 v[22:25], v[22:25], v[14:17], v[26:29]
	v_lshl_add_u64 v[38:39], s[2:3], 0, v[38:39]
	v_cvt_pk_fp8_f32 v63, v20, v21 op_sel:[0,0,1]
	v_and_b32_e32 v0, 16, v0
	ds_read_b128 v[26:29], v37 offset:8896
	v_mfma_f32_16x16x32_f16 v[22:25], v[42:45], v[6:9], v[22:25]
	ds_read_b128 v[42:45], v37 offset:13056
	v_cmp_lt_u32_e32 vcc, 1, v40
	s_waitcnt lgkmcnt(1)
	v_mfma_f32_16x16x32_f16 v[22:25], v[26:29], v[2:5], v[22:25]
	ds_read_b128 v[26:29], v37 offset:13120
	v_mfma_f32_16x16x32_f16 v[10:13], v[46:49], v[2:5], v[10:13]
	ds_read_b128 v[46:49], v37 offset:13184
	s_waitcnt lgkmcnt(2)
	v_mfma_f32_16x16x32_f16 v[42:45], v[42:45], v[30:33], 0
	s_waitcnt lgkmcnt(1)
	v_mfma_f32_16x16x32_f16 v[26:29], v[26:29], v[14:17], v[42:45]
	s_nop 2
	v_cvt_pk_fp8_f32 v62, v10, v11
	v_cvt_pk_fp8_f32 v62, v12, v13 op_sel:[0,0,1]
	s_nop 0
	ds_read_b128 v[42:45], v37 offset:13248
	s_waitcnt lgkmcnt(1)
	v_mfma_f32_16x16x32_f16 v[26:29], v[46:49], v[6:9], v[26:29]
	ds_read_b128 v[46:49], v37 offset:17408
	v_permlane16_swap_b32_e32 v62, v63
	s_waitcnt lgkmcnt(1)
	v_mfma_f32_16x16x32_f16 v[26:29], v[42:45], v[2:5], v[26:29]
	ds_read_b128 v[42:45], v37 offset:17472
	s_waitcnt lgkmcnt(1)
	v_mfma_f32_16x16x32_f16 v[46:49], v[46:49], v[30:33], 0
	s_waitcnt lgkmcnt(0)
	v_mfma_f32_16x16x32_f16 v[42:45], v[42:45], v[14:17], v[46:49]
	s_nop 5
	ds_read_b128 v[46:49], v37 offset:17600
	v_mfma_f32_16x16x32_f16 v[42:45], v[50:53], v[6:9], v[42:45]
	ds_read_b128 v[50:53], v37 offset:21760
	s_waitcnt lgkmcnt(1)
	v_mfma_f32_16x16x32_f16 v[42:45], v[46:49], v[2:5], v[42:45]
	ds_read_b128 v[46:49], v37 offset:21824
	s_waitcnt lgkmcnt(1)
	v_mfma_f32_16x16x32_f16 v[50:53], v[50:53], v[30:33], 0
	s_waitcnt lgkmcnt(0)
	v_mfma_f32_16x16x32_f16 v[46:49], v[46:49], v[14:17], v[50:53]
	s_nop 5
	ds_read_b128 v[50:53], v37 offset:21952
	v_mfma_f32_16x16x32_f16 v[46:49], v[54:57], v[6:9], v[46:49]
	ds_read_b128 v[54:57], v37 offset:26112
	ds_read_b128 v[58:61], v37 offset:26176
	ds_read_b128 v[10:13], v37 offset:26240
	s_waitcnt lgkmcnt(2)
	v_mfma_f32_16x16x32_f16 v[18:21], v[54:57], v[30:33], 0
	s_waitcnt lgkmcnt(1)
	v_mfma_f32_16x16x32_f16 v[18:21], v[58:61], v[14:17], v[18:21]
	v_mov_b32_e32 v58, v35
	v_cvt_pk_fp8_f32 v58, v42, v43
	v_mov_b32_e32 v59, v35
	v_mfma_f32_16x16x32_f16 v[46:49], v[50:53], v[2:5], v[46:49]
	v_and_b32_e32 v50, 8, v1
	v_mov_b32_e32 v51, v35
	v_lshl_add_u64 v[38:39], v[38:39], 0, v[50:51]
	ds_read_b128 v[50:53], v37 offset:26304
	s_waitcnt lgkmcnt(1)
	v_mfma_f32_16x16x32_f16 v[10:13], v[10:13], v[6:9], v[18:21]
	s_nop 2
	ds_read_b128 v[18:21], v37 offset:30464
	ds_read_b128 v[54:57], v37 offset:30528
	v_mov_b32_e32 v1, v35
	v_lshl_add_u64 v[0:1], v[38:39], 0, v[0:1]
	v_mov_b32_e32 v38, v35
	v_cvt_pk_fp8_f32 v38, v22, v23
	s_waitcnt lgkmcnt(1)
	v_mfma_f32_16x16x32_f16 v[18:21], v[18:21], v[30:33], 0
	v_mov_b32_e32 v39, v35
	v_cvt_pk_fp8_f32 v39, v26, v27
	v_cvt_pk_fp8_f32 v38, v24, v25 op_sel:[0,0,1]
	v_mfma_f32_16x16x32_f16 v[10:13], v[50:53], v[2:5], v[10:13]
	ds_read_b128 v[22:25], v37 offset:30592
	ds_read_b128 v[50:53], v37 offset:30656
	global_store_dwordx2 v[0:1], v[62:63], off
	v_cvt_pk_fp8_f32 v39, v28, v29 op_sel:[0,0,1]
	s_waitcnt lgkmcnt(2)
	v_mfma_f32_16x16x32_f16 v[18:21], v[54:57], v[14:17], v[18:21]
	ds_read_b128 v[26:29], v37 offset:34816
	ds_read_b128 v[54:57], v37 offset:34880
	v_cvt_pk_fp8_f32 v58, v44, v45 op_sel:[0,0,1]
	v_permlane16_swap_b32_e32 v38, v39
	s_waitcnt lgkmcnt(3)
	v_mfma_f32_16x16x32_f16 v[18:21], v[22:25], v[6:9], v[18:21]
	ds_read_b128 v[22:25], v37 offset:34944
	ds_read_b128 v[42:45], v37 offset:35008
	global_store_dwordx2 v[0:1], v[38:39], off offset:32
	v_mov_b32_e32 v38, v35
	s_waitcnt lgkmcnt(4)
	v_mfma_f32_16x16x32_f16 v[18:21], v[50:53], v[2:5], v[18:21]
	v_mov_b32_e32 v39, v35
	v_cvt_pk_fp8_f32 v59, v46, v47
	v_cvt_pk_fp8_f32 v38, v10, v11
	s_waitcnt lgkmcnt(3)
	v_mfma_f32_16x16x32_f16 v[26:29], v[26:29], v[30:33], 0
	v_cvt_pk_fp8_f32 v59, v48, v49 op_sel:[0,0,1]
	s_nop 1
	v_cvt_pk_fp8_f32 v39, v18, v19
	s_waitcnt lgkmcnt(2)
	v_mfma_f32_16x16x32_f16 v[14:17], v[54:57], v[14:17], v[26:29]
	v_cvt_pk_fp8_f32 v38, v12, v13 op_sel:[0,0,1]
	v_permlane16_swap_b32_e32 v58, v59
	v_cvt_pk_fp8_f32 v39, v20, v21 op_sel:[0,0,1]
	s_waitcnt lgkmcnt(1)
	v_mfma_f32_16x16x32_f16 v[6:9], v[22:25], v[6:9], v[14:17]
	global_store_dwordx2 v[0:1], v[58:59], off offset:64
	v_permlane16_swap_b32_e32 v38, v39
	global_store_dwordx2 v[0:1], v[38:39], off offset:96
	s_waitcnt lgkmcnt(0)
	v_mfma_f32_16x16x32_f16 v[0:3], v[42:45], v[2:5], v[6:9]
	s_and_saveexec_b64 s[2:3], vcc
	s_xor_b64 s[2:3], exec, s[2:3]
	s_cbranch_execz .LBB1_77
	s_load_dwordx2 s[4:5], s[0:1], 0x20
	v_lshlrev_b64 v[4:5], 5, v[34:35]
	v_lshlrev_b32_e32 v34, 4, v40
	s_waitcnt lgkmcnt(0)
	v_lshl_add_u64 v[4:5], s[4:5], 0, v[4:5]
	v_lshl_add_u64 v[4:5], v[4:5], 0, v[34:35]
	global_store_dwordx4 v[4:5], v[0:3], off offset:-32

	.amdhsa_kernel _Z13second_kernelPKfPKDF16_PDF16_PfS4_PKjPKiPiS9_
		.amdhsa_group_segment_fixed_size 40960
		.amdhsa_private_segment_fixed_size 0
		.amdhsa_kernarg_size 72
		.amdhsa_user_sgpr_count 2
		.amdhsa_user_sgpr_dispatch_ptr 0
		.amdhsa_user_sgpr_queue_ptr 0
		.amdhsa_user_sgpr_kernarg_segment_ptr 1
		.amdhsa_user_sgpr_dispatch_id 0
		.amdhsa_user_sgpr_kernarg_preload_length 0
		.amdhsa_user_sgpr_kernarg_preload_offset 0
		.amdhsa_user_sgpr_private_segment_size 0
		.amdhsa_uses_dynamic_stack 0
		.amdhsa_enable_private_segment 0
		.amdhsa_system_sgpr_workgroup_id_x 1
		.amdhsa_system_sgpr_workgroup_id_y 0
		.amdhsa_system_sgpr_workgroup_id_z 0
		.amdhsa_system_sgpr_workgroup_info 0
		.amdhsa_system_vgpr_workitem_id 0
		.amdhsa_next_free_vgpr 64
		.amdhsa_next_free_sgpr 24
		.amdhsa_accum_offset 64
		.amdhsa_reserve_vcc 1
		.amdhsa_float_round_mode_32 0
		.amdhsa_float_round_mode_16_64 0
		.amdhsa_float_denorm_mode_32 3
		.amdhsa_float_denorm_mode_16_64 3
		.amdhsa_dx10_clamp 1
		.amdhsa_ieee_mode 1
		.amdhsa_fp16_overflow 0
		.amdhsa_tg_split 0
		.amdhsa_exception_fp_ieee_invalid_op 0
		.amdhsa_exception_fp_denorm_src 0
		.amdhsa_exception_fp_ieee_div_zero 0
		.amdhsa_exception_fp_ieee_overflow 0
		.amdhsa_exception_fp_ieee_underflow 0
		.amdhsa_exception_fp_ieee_inexact 0
		.amdhsa_exception_int_div_zero 0
	.end_amdhsa_kernel

amdhsa.kernels:
  - .agpr_count:     0
    .args:
      - .actual_access:  read_only
        .address_space:  global
        .offset:         0
        .size:           8
        .value_kind:     global_buffer
      - .actual_access:  read_only
        .address_space:  global
        .offset:         8
        .size:           8
        .value_kind:     global_buffer
      - .actual_access:  read_only
        .address_space:  global
        .offset:         16
        .size:           8
        .value_kind:     global_buffer
      - .actual_access:  read_only
        .address_space:  global
        .offset:         24
        .size:           8
        .value_kind:     global_buffer
      - .actual_access:  read_only
        .address_space:  global
        .offset:         32
        .size:           8
        .value_kind:     global_buffer
      - .actual_access:  read_only
        .address_space:  global
        .offset:         40
        .size:           8
        .value_kind:     global_buffer
      - .actual_access:  read_only
        .address_space:  global
        .offset:         48
        .size:           8
        .value_kind:     global_buffer
      - .actual_access:  read_only
        .address_space:  global
        .offset:         56
        .size:           8
        .value_kind:     global_buffer
      - .actual_access:  read_only
        .address_space:  global
        .offset:         64
        .size:           8
        .value_kind:     global_buffer
      - .actual_access:  read_only
        .address_space:  global
        .offset:         72
        .size:           8
        .value_kind:     global_buffer
      - .actual_access:  read_only
        .address_space:  global
        .offset:         80
        .size:           8
        .value_kind:     global_buffer
      - .actual_access:  read_only
        .address_space:  global
        .offset:         88
        .size:           8
        .value_kind:     global_buffer
      - .actual_access:  read_only
        .address_space:  global
        .offset:         96
        .size:           8
        .value_kind:     global_buffer
      - .actual_access:  write_only
        .address_space:  global
        .offset:         104
        .size:           8
        .value_kind:     global_buffer
      - .actual_access:  write_only
        .address_space:  global
        .offset:         112
        .size:           8
        .value_kind:     global_buffer
      - .actual_access:  write_only
        .address_space:  global
        .offset:         120
        .size:           8
        .value_kind:     global_buffer
      - .actual_access:  write_only
        .address_space:  global
        .offset:         128
        .size:           8
        .value_kind:     global_buffer
      - .actual_access:  write_only
        .address_space:  global
        .offset:         136
        .size:           8
        .value_kind:     global_buffer
      - .actual_access:  write_only
        .address_space:  global
        .offset:         144
        .size:           8
        .value_kind:     global_buffer
      - .actual_access:  write_only
        .address_space:  global
        .offset:         152
        .size:           8
        .value_kind:     global_buffer
      - .actual_access:  write_only
        .address_space:  global
        .offset:         160
        .size:           8
        .value_kind:     global_buffer
      - .actual_access:  write_only
        .address_space:  global
        .offset:         168
        .size:           8
        .value_kind:     global_buffer
      - .actual_access:  read_only
        .address_space:  global
        .offset:         176
        .size:           8
        .value_kind:     global_buffer
    .group_segment_fixed_size: 29696
    .kernarg_segment_align: 8
    .kernarg_segment_size: 184
    .language:       OpenCL C
    .language_version:
      - 2
      - 0
    .max_flat_workgroup_size: 512
    .name:           _Z12front_kernelPKiS0_PKfS2_S2_S2_S2_S2_S2_S2_S2_S2_S2_PjS3_PiS4_PDF16_PfS6_S4_S5_S0_
    .private_segment_fixed_size: 0
    .sgpr_count:     30
    .sgpr_spill_count: 0
    .symbol:         _Z12front_kernelPKiS0_PKfS2_S2_S2_S2_S2_S2_S2_S2_S2_S2_PjS3_PiS4_PDF16_PfS6_S4_S5_S0_.kd
    .uniform_work_group_size: 1
    .uses_dynamic_stack: false
    .vgpr_count:     80
    .vgpr_spill_count: 0
    .wavefront_size: 64
  - .agpr_count:     0
    .args:
      - .actual_access:  read_only
        .address_space:  global
        .offset:         0
        .size:           8
        .value_kind:     global_buffer
      - .actual_access:  read_only
        .address_space:  global
        .offset:         8
        .size:           8
        .value_kind:     global_buffer
      - .actual_access:  write_only
        .address_space:  global
        .offset:         16
        .size:           8
        .value_kind:     global_buffer
      - .actual_access:  write_only
        .address_space:  global
        .offset:         24
        .size:           8
        .value_kind:     global_buffer
      - .actual_access:  write_only
        .address_space:  global
        .offset:         32
        .size:           8
        .value_kind:     global_buffer
      - .actual_access:  read_only
        .address_space:  global
        .offset:         40
        .size:           8
        .value_kind:     global_buffer
      - .actual_access:  read_only
        .address_space:  global
        .offset:         48
        .size:           8
        .value_kind:     global_buffer
      - .actual_access:  write_only
        .address_space:  global
        .offset:         56
        .size:           8
        .value_kind:     global_buffer
      - .actual_access:  write_only
        .address_space:  global
        .offset:         64
        .size:           8
        .value_kind:     global_buffer
    .group_segment_fixed_size: 40960
    .kernarg_segment_align: 8
    .kernarg_segment_size: 72
    .language:       OpenCL C
    .language_version:
      - 2
      - 0
    .max_flat_workgroup_size: 512
    .name:           _Z13second_kernelPKfPKDF16_PDF16_PfS4_PKjPKiPiS9_
    .private_segment_fixed_size: 0
    .sgpr_count:     30
    .sgpr_spill_count: 0
    .symbol:         _Z13second_kernelPKfPKDF16_PDF16_PfS4_PKjPKiPiS9_.kd
    .uniform_work_group_size: 1
    .uses_dynamic_stack: false
    .vgpr_count:     64
    .vgpr_spill_count: 0
    .wavefront_size: 64
  - .agpr_count:     0
    .args:
      - .actual_access:  read_only
        .address_space:  global
        .offset:         0
        .size:           8
        .value_kind:     global_buffer
      - .actual_access:  read_only
        .address_space:  global
        .offset:         8
        .size:           8
        .value_kind:     global_buffer
      - .actual_access:  read_only
        .address_space:  global
        .offset:         16
        .size:           8
        .value_kind:     global_buffer
      - .actual_access:  read_only
        .address_space:  global
        .offset:         24
        .size:           8
        .value_kind:     global_buffer
      - .actual_access:  read_only
        .address_space:  global
        .offset:         32
        .size:           8
        .value_kind:     global_buffer
      - .actual_access:  read_only
        .address_space:  global
        .offset:         40
        .size:           8
        .value_kind:     global_buffer
      - .actual_access:  read_only
        .address_space:  global
        .offset:         48
        .size:           8
        .value_kind:     global_buffer
      - .actual_access:  write_only
        .address_space:  global
        .offset:         56
        .size:           8
        .value_kind:     global_buffer
      - .actual_access:  write_only
        .address_space:  global
        .offset:         64
        .size:           8
        .value_kind:     global_buffer
      - .actual_access:  write_only
        .address_space:  global
        .offset:         72
        .size:           8
        .value_kind:     global_buffer
      - .offset:         80
        .size:           4
        .value_kind:     by_value
    .group_segment_fixed_size: 10240
    .kernarg_segment_align: 8
    .kernarg_segment_size: 84
    .language:       OpenCL C
    .language_version:
      - 2
      - 0
    .max_flat_workgroup_size: 256
    .name:           _Z11agg1_kernelPKDF16_PKfS2_PKiS4_S2_S2_PDF16_PfS6_i
    .private_segment_fixed_size: 0
    .sgpr_count:     50
    .sgpr_spill_count: 0
    .symbol:         _Z11agg1_kernelPKDF16_PKfS2_PKiS4_S2_S2_PDF16_PfS6_i.kd
    .uniform_work_group_size: 1
    .uses_dynamic_stack: false
    .vgpr_count:     70
    .vgpr_spill_count: 0
    .wavefront_size: 64
  - .agpr_count:     0
    .args:
      - .actual_access:  read_only
        .address_space:  global
        .offset:         0
        .size:           8
        .value_kind:     global_buffer
      - .actual_access:  read_only
        .address_space:  global
        .offset:         8
        .size:           8
        .value_kind:     global_buffer
      - .actual_access:  read_only
        .address_space:  global
        .offset:         16
        .size:           8
        .value_kind:     global_buffer
      - .actual_access:  read_only
        .address_space:  global
        .offset:         24
        .size:           8
        .value_kind:     global_buffer
      - .actual_access:  read_only
        .address_space:  global
        .offset:         32
        .size:           8
        .value_kind:     global_buffer
      - .actual_access:  write_only
        .address_space:  global
        .offset:         40
        .size:           8
        .value_kind:     global_buffer
      - .offset:         48
        .size:           4
        .value_kind:     by_value
    .group_segment_fixed_size: 0
    .kernarg_segment_align: 8
    .kernarg_segment_size: 52
    .language:       OpenCL C
    .language_version:
      - 2
      - 0
    .max_flat_workgroup_size: 256
    .name:           _Z13stats2_kernelPKiS0_PKfS2_S0_P15HIP_vector_typeIfLj4EEi
    .private_segment_fixed_size: 0
    .sgpr_count:     38
    .sgpr_spill_count: 0
    .symbol:         _Z13stats2_kernelPKiS0_PKfS2_S0_P15HIP_vector_typeIfLj4EEi.kd
    .uniform_work_group_size: 1
    .uses_dynamic_stack: false
    .vgpr_count:     32
    .vgpr_spill_count: 0
    .wavefront_size: 64
  - .agpr_count:     0
    .args:
      - .actual_access:  read_only
        .address_space:  global
        .offset:         0
        .size:           8
        .value_kind:     global_buffer
      - .actual_access:  read_only
        .address_space:  global
        .offset:         8
        .size:           8
        .value_kind:     global_buffer
      - .actual_access:  read_only
        .address_space:  global
        .offset:         16
        .size:           8
        .value_kind:     global_buffer
      - .actual_access:  read_only
        .address_space:  global
        .offset:         24
        .size:           8
        .value_kind:     global_buffer
      - .actual_access:  read_only
        .address_space:  global
        .offset:         32
        .size:           8
        .value_kind:     global_buffer
      - .actual_access:  write_only
        .address_space:  global
        .offset:         40
        .size:           8
        .value_kind:     global_buffer
      - .offset:         48
        .size:           4
        .value_kind:     by_value
    .group_segment_fixed_size: 70752
    .kernarg_segment_align: 8
    .kernarg_segment_size: 52
    .language:       OpenCL C
    .language_version:
      - 2
      - 0
    .max_flat_workgroup_size: 1024
    .name:           _Z12pool2_kernelPKjPKiPKfPK15HIP_vector_typeIfLj4EEPKDF16_Pfi
    .private_segment_fixed_size: 0
    .sgpr_count:     26
    .sgpr_spill_count: 0
    .symbol:         _Z12pool2_kernelPKjPKiPKfPK15HIP_vector_typeIfLj4EEPKDF16_Pfi.kd
    .uniform_work_group_size: 1
    .uses_dynamic_stack: false
    .vgpr_count:     128
    .vgpr_spill_count: 0
    .wavefront_size: 64
  - .agpr_count:     0
    .args:
      - .actual_access:  read_only
        .address_space:  global
        .offset:         0
        .size:           8
        .value_kind:     global_buffer
      - .actual_access:  read_only
        .address_space:  global
        .offset:         8
        .size:           8
        .value_kind:     global_buffer
      - .actual_access:  read_only
        .address_space:  global
        .offset:         16
        .size:           8
        .value_kind:     global_buffer
      - .actual_access:  read_only
        .address_space:  global
        .offset:         24
        .size:           8
        .value_kind:     global_buffer
      - .actual_access:  read_only
        .address_space:  global
        .offset:         32
        .size:           8
        .value_kind:     global_buffer
      - .actual_access:  read_only
        .address_space:  global
        .offset:         40
        .size:           8
        .value_kind:     global_buffer
      - .actual_access:  read_only
        .address_space:  global
        .offset:         48
        .size:           8
        .value_kind:     global_buffer
      - .actual_access:  read_only
        .address_space:  global
        .offset:         56
        .size:           8
        .value_kind:     global_buffer
      - .actual_access:  write_only
        .address_space:  global
        .offset:         64
        .size:           8
        .value_kind:     global_buffer
    .group_segment_fixed_size: 9472
    .kernarg_segment_align: 8
    .kernarg_segment_size: 72
    .language:       OpenCL C
    .language_version:
      - 2
      - 0
    .max_flat_workgroup_size: 1024
    .name:           _Z10mlp_kernelPKfPKiS0_S0_S0_S0_S0_S0_Pf
    .private_segment_fixed_size: 0
    .sgpr_count:     76
    .sgpr_spill_count: 0
    .symbol:         _Z10mlp_kernelPKfPKiS0_S0_S0_S0_S0_S0_Pf.kd
    .uniform_work_group_size: 1
    .uses_dynamic_stack: false
    .vgpr_count:     77
    .vgpr_spill_count: 0
    .wavefront_size: 64
